# speedup vs baseline: 1.0122x; 1.0122x over previous
.Lmsk_8179:
	v_readfirstlane_b32 s54, v0
	v_lshlrev_b32_e32 v160, 1, v210
	s_or_b32 s50, s12, s27
	s_lshr_b32 s54, s54, 6
	s_lshl_b32 s54, s54, 5
	s_add_u32 s50, s50, s54
	s_addc_u32 s51, s13, 0
	s_lshl_b64 s[50:51], s[50:51], 11
	s_add_u32 s50, s4, s50
	s_addc_u32 s51, s5, s51
	s_lshl_b32 s54, s33, 1
	s_add_u32 s50, s50, s54
	s_addc_u32 s51, s51, 0
	global_load_dwordx4 v[156:159], v160, s[50:51]
	global_load_dwordx4 v[152:155], v160, s[50:51] offset:32
	global_load_dwordx4 v[148:151], v160, s[50:51] offset:64
	global_load_dwordx4 v[144:147], v160, s[50:51] offset:96
	v_exp_f32_e32 v86, v86
	v_exp_f32_e32 v87, v87
	v_exp_f32_e32 v88, v88
	v_exp_f32_e32 v89, v89
	s_waitcnt lgkmcnt(10)
	s_cmp_lt_u32 s55, 4
	s_cbranch_scc1 .Lmsk_8188
	v_mfma_f32_32x32x16_f16 v[2:17], v[138:141], v[102:105], v[2:17]

.Lmsk_8416:
	s_and_saveexec_b64 s[2:3], s[0:1]
	v_add_f32_e32 v34, v51, v34
	ds_write_b32 v223, v34 offset:49280
	s_or_b64 exec, exec, s[2:3]
	s_waitcnt lgkmcnt(0)
	ds_read_b128 v[34:37], v50 offset:49280
	ds_read_b128 v[38:41], v50 offset:49312
	s_lshl_b64 s[2:3], s[14:15], 1
	s_add_u32 s2, s10, s2
	s_addc_u32 s3, s11, s3
	s_waitcnt lgkmcnt(1)
	v_rcp_f32_e32 v42, v34
	v_rcp_f32_e32 v43, v35
	s_lshl_b32 s6, s34, 12
	s_add_i32 s6, s6, 0
	v_lshlrev_b32_e32 v230, 1, v222
	v_lshlrev_b32_e32 v231, 9, v211
	v_rcp_f32_e32 v44, v36
	v_rcp_f32_e32 v45, v37
	s_waitcnt lgkmcnt(0)
	v_rcp_f32_e32 v46, v38
	ds_read_b128 v[34:37], v50 offset:49344
	v_rcp_f32_e32 v47, v39
	v_rcp_f32_e32 v48, v40
	v_rcp_f32_e32 v49, v41
	ds_read_b128 v[38:41], v50 offset:49376
	v_add3_u32 v50, s6, v230, v231
	v_fma_mixlo_f16 v2, v2, v42, 0
	ds_write_b16 v50, v2 offset:51200
	v_fma_mixlo_f16 v2, v18, v42, 0
	ds_write_b16 v50, v2 offset:51264
	v_fma_mixlo_f16 v2, v3, v43, 0
	ds_write_b16 v50, v2 offset:51328
	v_fma_mixlo_f16 v2, v19, v43, 0
	ds_write_b16 v50, v2 offset:51392
	v_fma_mixlo_f16 v2, v4, v44, 0
	ds_write_b16 v50, v2 offset:51456
	v_fma_mixlo_f16 v2, v20, v44, 0
	ds_write_b16 v50, v2 offset:51520
	v_fma_mixlo_f16 v2, v5, v45, 0
	ds_write_b16 v50, v2 offset:51584
	v_fma_mixlo_f16 v2, v21, v45, 0
	ds_write_b16 v50, v2 offset:51648
	v_fma_mixlo_f16 v2, v6, v46, 0
	ds_write_b16 v50, v2 offset:52224
	v_fma_mixlo_f16 v2, v22, v46, 0
	ds_write_b16 v50, v2 offset:52288
	v_fma_mixlo_f16 v2, v7, v47, 0
	ds_write_b16 v50, v2 offset:52352
	v_fma_mixlo_f16 v2, v23, v47, 0
	s_waitcnt lgkmcnt(12)
	v_rcp_f32_e32 v34, v34
	ds_write_b16 v50, v2 offset:52416
	v_fma_mixlo_f16 v2, v8, v48, 0
	ds_write_b16 v50, v2 offset:52480
	v_fma_mixlo_f16 v2, v24, v48, 0
	v_rcp_f32_e32 v35, v35
	ds_write_b16 v50, v2 offset:52544
	v_fma_mixlo_f16 v2, v9, v49, 0
	ds_write_b16 v50, v2 offset:52608
	v_fma_mixlo_f16 v2, v25, v49, 0
	v_rcp_f32_e32 v36, v36
	ds_write_b16 v50, v2 offset:52672
	v_fma_mixlo_f16 v2, v10, v34, 0
	ds_write_b16 v50, v2 offset:53248
	v_fma_mixlo_f16 v2, v26, v34, 0
	v_rcp_f32_e32 v37, v37
	ds_write_b16 v50, v2 offset:53312
	v_fma_mixlo_f16 v2, v11, v35, 0
	ds_write_b16 v50, v2 offset:53376
	v_fma_mixlo_f16 v2, v27, v35, 0
	s_waitcnt lgkmcnt(14)
	v_rcp_f32_e32 v38, v38
	ds_write_b16 v50, v2 offset:53440
	v_fma_mixlo_f16 v2, v12, v36, 0
	ds_write_b16 v50, v2 offset:53504
	v_fma_mixlo_f16 v2, v28, v36, 0
	v_rcp_f32_e32 v39, v39
	ds_write_b16 v50, v2 offset:53568
	v_fma_mixlo_f16 v2, v13, v37, 0
	ds_write_b16 v50, v2 offset:53632
	v_fma_mixlo_f16 v2, v29, v37, 0
	v_rcp_f32_e32 v40, v40
	ds_write_b16 v50, v2 offset:53696
	v_fma_mixlo_f16 v2, v14, v38, 0
	ds_write_b16 v50, v2 offset:54272
	v_fma_mixlo_f16 v2, v30, v38, 0
	v_rcp_f32_e32 v41, v41
	ds_write_b16 v50, v2 offset:54336
	v_fma_mixlo_f16 v2, v15, v39, 0
	ds_write_b16 v50, v2 offset:54400
	v_fma_mixlo_f16 v2, v31, v39, 0
	ds_write_b16 v50, v2 offset:54464
	v_fma_mixlo_f16 v2, v16, v40, 0
	ds_write_b16 v50, v2 offset:54528
	v_fma_mixlo_f16 v2, v32, v40, 0
	ds_write_b16 v50, v2 offset:54592
	v_fma_mixlo_f16 v2, v17, v41, 0
	ds_write_b16 v50, v2 offset:54656
	v_fma_mixlo_f16 v2, v33, v41, 0
	ds_write_b16 v50, v2 offset:54720
	v_and_b32_e32 v2, 56, v209
	s_lshl_b32 s22, s33, 1
	v_lshrrev_b32_e32 v36, 3, v207
	v_lshlrev_b32_e32 v220, 1, v2
	s_add_u32 s2, s2, s22
	v_add_u32_e32 v14, s6, v220
	v_lshlrev_b32_e32 v232, 7, v36
	s_addc_u32 s3, s3, 0
	s_waitcnt lgkmcnt(0)
	v_mov_b32_e32 v221, 0
	v_add_u32_e32 v2, v14, v232
	v_or_b32_e32 v37, 8, v36
	v_lshl_add_u64 v[10:11], s[2:3], 0, v[220:221]
	ds_read_b128 v[2:5], v2 offset:51200
	v_lshlrev_b32_e32 v6, 11, v36
	v_mov_b32_e32 v7, v221
	v_lshlrev_b32_e32 v233, 7, v37
	v_readfirstlane_b32 s8, v0
	v_lshl_add_u64 v[12:13], v[10:11], 0, v[6:7]
	v_add_u32_e32 v6, v14, v233
	s_lshr_b32 s23, s8, 6
	ds_read_b128 v[6:9], v6 offset:51200
	s_or_b32 s2, s12, s27
	s_lshl_b32 s12, s23, 5
	s_add_u32 s6, s2, s12
	s_addc_u32 s7, s13, 0
	s_waitcnt lgkmcnt(1)
	global_store_dwordx4 v[12:13], v[2:5], off sc1
	v_or_b32_e32 v38, 16, v36
	s_lshl_b64 s[2:3], s[6:7], 11
	v_lshlrev_b32_e32 v2, 11, v37
	v_mov_b32_e32 v3, v221
	v_lshl_add_u64 v[2:3], v[10:11], 0, v[2:3]
	v_lshlrev_b32_e32 v234, 7, v38
	s_add_u32 s2, s4, s2
	s_waitcnt lgkmcnt(0)
	global_store_dwordx4 v[2:3], v[6:9], off sc1
	v_add_u32_e32 v2, v14, v234
	v_or_b32_e32 v39, 24, v36
	s_addc_u32 s3, s5, s3
	ds_read_b128 v[2:5], v2 offset:51200
	v_lshlrev_b32_e32 v6, 11, v38
	v_mov_b32_e32 v7, v221
	v_lshlrev_b32_e32 v235, 7, v39
	s_add_u32 s2, s2, s22
	v_lshl_add_u64 v[12:13], v[10:11], 0, v[6:7]
	v_add_u32_e32 v6, v14, v235
	s_addc_u32 s3, s3, 0
	s_lshl_b32 s4, s8, 4
	ds_read_b128 v[6:9], v6 offset:51200
	s_and_b32 s4, s4, 0xfffff000
	s_add_u32 s4, s30, s4
	s_addc_u32 s5, s31, 0
	s_lshr_b32 s9, s8, 2
	s_waitcnt lgkmcnt(1)
	global_store_dwordx4 v[12:13], v[2:5], off sc1
	v_and_or_b32 v0, s9, 48, v1
	s_lshl_b32 s9, s23, 10
	v_lshlrev_b32_e32 v2, 11, v39
	v_mov_b32_e32 v3, v221
	v_lshl_add_u64 v[2:3], v[10:11], 0, v[2:3]
	v_lshlrev_b32_e32 v0, 6, v0
	v_mov_b32_e32 v1, v221
	s_cmp_lg_u32 0, -1
	s_waitcnt lgkmcnt(0)
	global_store_dwordx4 v[2:3], v[6:9], off sc1
	v_lshl_add_u64 v[0:1], s[4:5], 0, v[0:1]
	s_cselect_b32 s4, 0, 0
	s_waitcnt lgkmcnt(0)
	s_barrier
	v_lshlrev_b32_e32 v2, 1, v208
	v_mov_b32_e32 v3, v221
	s_add_i32 s25, s4, s9
	v_lshl_add_u64 v[208:209], v[0:1], 0, v[2:3]
	s_addk_i32 s25, 0x6000
	s_mov_b32 s4, m0
	s_mov_b32 m0, s25
	s_nop 0
	global_load_lds_dwordx4 v[208:209], off
	s_mov_b32 m0, s4
	v_lshlrev_b32_e32 v0, 1, v210
	v_mov_b32_e32 v0, v221
	v_mov_b32_e32 v1, v221
	v_mov_b32_e32 v2, v221
	v_mov_b32_e32 v4, v221
	v_mov_b32_e32 v5, v221
	v_mov_b32_e32 v6, v221
	v_mov_b32_e32 v7, v221
	v_mov_b32_e32 v8, v221
	v_mov_b32_e32 v9, v221
	v_mov_b32_e32 v10, v221
	v_mov_b32_e32 v11, v221
	v_mov_b32_e32 v12, v221
	v_mov_b32_e32 v13, v221
	v_mov_b32_e32 v14, v221
	v_mov_b32_e32 v15, v221
	s_waitcnt vmcnt(5) lgkmcnt(0)
	s_barrier
	ds_read_b128 v[32:35], v224
	s_cmp_lg_u32 s26, 0
	s_waitcnt lgkmcnt(0)
	v_mfma_f32_32x32x16_f16 v[16:31], v[32:35], v[156:159], v[0:15]
	ds_read_b128 v[32:35], v224 offset:512
	s_cselect_b64 s[2:3], -1, 0
	v_lshlrev_b32_e32 v239, 10, v36
	v_lshlrev_b32_e32 v238, 10, v37
	v_lshlrev_b32_e32 v237, 10, v38
	v_lshlrev_b32_e32 v236, 10, v39
	v_or_b32_e32 v221, s12, v222
	s_waitcnt lgkmcnt(0)
	v_mfma_f32_32x32x16_f16 v[0:15], v[32:35], v[156:159], v[0:15]
	ds_read_b128 v[32:35], v224 offset:2048
	s_and_b64 vcc, exec, s[2:3]
	s_waitcnt lgkmcnt(0)
	v_mfma_f32_32x32x16_f16 v[16:31], v[32:35], v[152:155], v[16:31]
	ds_read_b128 v[32:35], v224 offset:2560
	s_waitcnt lgkmcnt(0)
	v_mfma_f32_32x32x16_f16 v[0:15], v[32:35], v[152:155], v[0:15]
	ds_read_b128 v[32:35], v224 offset:4096
	s_waitcnt lgkmcnt(0)
	v_mfma_f32_32x32x16_f16 v[16:31], v[32:35], v[148:151], v[16:31]
	ds_read_b128 v[32:35], v224 offset:4608
	s_waitcnt lgkmcnt(0)
	v_mfma_f32_32x32x16_f16 v[0:15], v[32:35], v[148:151], v[0:15]
	ds_read_b128 v[32:35], v224 offset:6144
	s_waitcnt lgkmcnt(0)
	v_mfma_f32_32x32x16_f16 v[16:31], v[32:35], v[144:147], v[16:31]
	ds_read_b128 v[32:35], v224 offset:6656
	s_waitcnt lgkmcnt(0)
	v_mfma_f32_32x32x16_f16 v[0:15], v[32:35], v[144:147], v[0:15]
	s_nop 15
	s_nop 7
	s_cbranch_vccnz .LBB2_119
	v_readfirstlane_b32 s12, v221
	s_cmp_lt_i32 s12, 0
	s_cbranch_scc1 .LBB2_111
	s_cmp_gt_u32 s12, 31
	s_cbranch_scc1 .LBB2_112
	v_mov_b32_e32 v32, 0xff800000
	v_cmp_lt_u32_e32 vcc, v227, v221
	v_or_b32_e32 v33, 2, v227
	s_mov_b32 s13, 0xff800000
	v_cndmask_b32_e32 v17, v32, v17, vcc
	v_cmp_le_u32_e32 vcc, v227, v221
	s_nop 1
	v_cndmask_b32_e32 v16, v32, v16, vcc
	v_cmp_le_u32_e32 vcc, v33, v221
	v_or_b32_e32 v33, 3, v227
	s_nop 0
	v_cndmask_b32_e32 v18, v32, v18, vcc
	v_cmp_le_u32_e32 vcc, v33, v221
	v_or_b32_e32 v33, 8, v227
	s_nop 0
	v_cndmask_b32_e32 v19, v32, v19, vcc
	v_cmp_le_u32_e32 vcc, v33, v221
	v_or_b32_e32 v33, 9, v227
	s_nop 0
	v_cndmask_b32_e32 v20, v32, v20, vcc
	v_cmp_le_u32_e32 vcc, v33, v221
	v_or_b32_e32 v33, 10, v227
	s_nop 0
	v_cndmask_b32_e32 v21, v32, v21, vcc
	v_cmp_le_u32_e32 vcc, v33, v221
	v_or_b32_e32 v33, 11, v227
	s_nop 0
	v_cndmask_b32_e32 v22, v32, v22, vcc
	v_cmp_le_u32_e32 vcc, v33, v221
	v_or_b32_e32 v33, 16, v227
	s_nop 0
	v_cndmask_b32_e32 v23, v32, v23, vcc
	v_cmp_le_u32_e32 vcc, v33, v221
	v_or_b32_e32 v33, 17, v227
	s_nop 0
	v_cndmask_b32_e32 v24, v32, v24, vcc
	v_cmp_le_u32_e32 vcc, v33, v221
	v_or_b32_e32 v33, 18, v227
	s_nop 0
	v_cndmask_b32_e32 v25, v32, v25, vcc
	v_cmp_le_u32_e32 vcc, v33, v221
	v_or_b32_e32 v33, 19, v227
	s_nop 0
	v_cndmask_b32_e32 v26, v32, v26, vcc
	v_cmp_le_u32_e32 vcc, v33, v221
	v_or_b32_e32 v33, 24, v227
	s_nop 0
	v_cndmask_b32_e32 v27, v32, v27, vcc
	v_cmp_le_u32_e32 vcc, v33, v221
	v_or_b32_e32 v33, 25, v227
	s_nop 0
	v_cndmask_b32_e32 v28, v32, v28, vcc
	v_cmp_le_u32_e32 vcc, v33, v221
	v_or_b32_e32 v33, 26, v227
	s_nop 0
	v_cndmask_b32_e32 v29, v32, v29, vcc
	v_cmp_le_u32_e32 vcc, v33, v221
	s_nop 1
	v_cndmask_b32_e32 v30, v32, v30, vcc
	v_or_b32_e32 v32, 27, v227
	v_cmp_gt_u32_e32 vcc, v32, v221
	s_and_saveexec_b64 s[4:5], vcc
	v_mov_b32_e32 v31, s13
	s_or_b64 exec, exec, s[4:5]
	s_branch .LBB2_112
